# loop-edge edit: in the four GEMM K loops the trip counter / pointer increments and exit compare moved from behind the trip's closing barrier to in front of it
# speedup vs baseline: 1.0112x; 1.0018x over previous
.LBB0_220:
	ds_read_b128 v[128:131], v172
	ds_read_b128 v[132:135], v172 offset:1024
	ds_read_b128 v[154:157], v172 offset:2048
	ds_read_b128 v[158:161], v172 offset:3072
	ds_read_b128 v[162:165], v173
	ds_read_b128 v[176:179], v173 offset:1024
	ds_read_b128 v[180:183], v173 offset:2048
	ds_read_b128 v[188:191], v173 offset:3072
	s_add_u32 s58, s56, 0x80
	s_addc_u32 s59, s57, 0
	s_cmp_eq_u32 s82, 12
	s_cselect_b32 s61, s9, s59
	s_cselect_b32 s60, s47, s58
	s_cselect_b32 s59, s45, s81
	s_cselect_b32 s58, s55, s80
	v_lshl_add_u64 v[166:167], s[56:57], 0, v[152:153]
	s_add_i32 m0, s69, 0xc000
	ds_read_b128 v[192:195], v174
	ds_read_b128 v[196:199], v174 offset:1024
	ds_read_b128 v[200:203], v174 offset:2048
	ds_read_b128 v[204:207], v174 offset:3072
	ds_read_b128 v[208:211], v174 offset:4096
	ds_read_b128 v[212:215], v174 offset:5120
	ds_read_b128 v[216:219], v174 offset:6144
	ds_read_b128 v[220:223], v174 offset:7168
	global_load_lds_dwordx4 v[166:167], off
	v_lshl_add_u64 v[166:167], s[56:57], 0, v[150:151]
	s_add_i32 m0, s69, 0xe000
	s_nop 0
	global_load_lds_dwordx4 v[166:167], off
	s_waitcnt vmcnt(8)
	s_waitcnt lgkmcnt(0)
	s_barrier
	s_setprio 1
	s_waitcnt lgkmcnt(0)
	v_mfma_f32_16x16x32_bf16 v[124:127], v[128:131], v[192:195], v[124:127]
	v_mfma_f32_16x16x32_bf16 v[120:123], v[154:157], v[192:195], v[120:123]
	v_mfma_f32_16x16x32_bf16 v[116:119], v[128:131], v[200:203], v[116:119]
	v_mfma_f32_16x16x32_bf16 v[112:115], v[154:157], v[200:203], v[112:115]
	v_mfma_f32_16x16x32_bf16 v[108:111], v[128:131], v[208:211], v[108:111]
	v_mfma_f32_16x16x32_bf16 v[104:107], v[154:157], v[208:211], v[104:107]
	v_mfma_f32_16x16x32_bf16 v[100:103], v[128:131], v[216:219], v[100:103]
	v_mfma_f32_16x16x32_bf16 v[96:99], v[154:157], v[216:219], v[96:99]
	v_mfma_f32_16x16x32_bf16 v[124:127], v[132:135], v[196:199], v[124:127]
	v_mfma_f32_16x16x32_bf16 v[120:123], v[158:161], v[196:199], v[120:123]
	v_mfma_f32_16x16x32_bf16 v[116:119], v[132:135], v[204:207], v[116:119]
	v_mfma_f32_16x16x32_bf16 v[112:115], v[158:161], v[204:207], v[112:115]
	v_mfma_f32_16x16x32_bf16 v[108:111], v[132:135], v[212:215], v[108:111]
	v_mfma_f32_16x16x32_bf16 v[104:107], v[158:161], v[212:215], v[104:107]
	v_mfma_f32_16x16x32_bf16 v[100:103], v[132:135], v[220:223], v[100:103]
	v_mfma_f32_16x16x32_bf16 v[96:99], v[158:161], v[220:223], v[96:99]
	s_setprio 0
	s_setprio 1
	v_mfma_f32_16x16x32_bf16 v[60:63], v[162:165], v[192:195], v[60:63]
	v_mfma_f32_16x16x32_bf16 v[56:59], v[180:183], v[192:195], v[56:59]
	v_mfma_f32_16x16x32_bf16 v[52:55], v[162:165], v[200:203], v[52:55]
	v_mfma_f32_16x16x32_bf16 v[48:51], v[180:183], v[200:203], v[48:51]
	v_mfma_f32_16x16x32_bf16 v[44:47], v[162:165], v[208:211], v[44:47]
	v_mfma_f32_16x16x32_bf16 v[40:43], v[180:183], v[208:211], v[40:43]
	v_mfma_f32_16x16x32_bf16 v[36:39], v[162:165], v[216:219], v[36:39]
	v_mfma_f32_16x16x32_bf16 v[32:35], v[180:183], v[216:219], v[32:35]
	v_mfma_f32_16x16x32_bf16 v[60:63], v[176:179], v[196:199], v[60:63]
	v_mfma_f32_16x16x32_bf16 v[56:59], v[188:191], v[196:199], v[56:59]
	v_mfma_f32_16x16x32_bf16 v[52:55], v[176:179], v[204:207], v[52:55]
	v_mfma_f32_16x16x32_bf16 v[48:51], v[188:191], v[204:207], v[48:51]
	v_mfma_f32_16x16x32_bf16 v[44:47], v[176:179], v[212:215], v[44:47]
	v_mfma_f32_16x16x32_bf16 v[40:43], v[188:191], v[212:215], v[40:43]
	v_mfma_f32_16x16x32_bf16 v[36:39], v[176:179], v[220:223], v[36:39]
	v_mfma_f32_16x16x32_bf16 v[32:35], v[188:191], v[220:223], v[32:35]
	s_setprio 0
	s_barrier
	s_add_i32 s83, s77, s68
	v_lshl_add_u64 v[166:167], s[58:59], 0, v[136:137]
	s_mov_b32 m0, s83
	ds_read_b128 v[192:195], v174 offset:16384
	ds_read_b128 v[196:199], v174 offset:17408
	ds_read_b128 v[200:203], v174 offset:18432
	ds_read_b128 v[204:207], v174 offset:19456
	ds_read_b128 v[208:211], v174 offset:20480
	ds_read_b128 v[212:215], v174 offset:21504
	ds_read_b128 v[216:219], v174 offset:22528
	ds_read_b128 v[220:223], v174 offset:23552
	global_load_lds_dwordx4 v[166:167], off
	s_add_i32 m0, s83, 0x2000
	s_add_u32 s84, s58, 0x40000
	v_lshl_add_u64 v[184:185], s[58:59], 0, v[142:143]
	s_addc_u32 s85, s59, 0
	s_add_i32 s83, s78, s68
	global_load_lds_dwordx4 v[184:185], off
	v_lshl_add_u64 v[224:225], s[84:85], 0, v[136:137]
	s_mov_b32 m0, s83
	v_lshl_add_u64 v[226:227], s[60:61], 0, v[144:145]
	global_load_lds_dwordx4 v[224:225], off
	v_lshl_add_u64 v[224:225], s[84:85], 0, v[142:143]
	s_add_i32 m0, s83, 0x2000
	s_nop 0
	global_load_lds_dwordx4 v[224:225], off
	v_lshl_add_u64 v[224:225], s[60:61], 0, v[138:139]
	s_mov_b32 m0, s69
	s_nop 0
	global_load_lds_dwordx4 v[224:225], off
	s_mov_b32 m0, s70
	s_nop 0
	global_load_lds_dwordx4 v[226:227], off
	s_waitcnt vmcnt(8)
	s_waitcnt lgkmcnt(0)
	s_barrier
	s_setprio 1
	s_waitcnt lgkmcnt(0)
	v_mfma_f32_16x16x32_bf16 v[92:95], v[128:131], v[192:195], v[92:95]
	v_mfma_f32_16x16x32_bf16 v[88:91], v[154:157], v[192:195], v[88:91]
	v_mfma_f32_16x16x32_bf16 v[84:87], v[128:131], v[200:203], v[84:87]
	v_mfma_f32_16x16x32_bf16 v[80:83], v[154:157], v[200:203], v[80:83]
	v_mfma_f32_16x16x32_bf16 v[76:79], v[128:131], v[208:211], v[76:79]
	v_mfma_f32_16x16x32_bf16 v[72:75], v[154:157], v[208:211], v[72:75]
	v_mfma_f32_16x16x32_bf16 v[68:71], v[128:131], v[216:219], v[68:71]
	v_mfma_f32_16x16x32_bf16 v[64:67], v[154:157], v[216:219], v[64:67]
	v_mfma_f32_16x16x32_bf16 v[92:95], v[132:135], v[196:199], v[92:95]
	v_mfma_f32_16x16x32_bf16 v[88:91], v[158:161], v[196:199], v[88:91]
	v_mfma_f32_16x16x32_bf16 v[84:87], v[132:135], v[204:207], v[84:87]
	v_mfma_f32_16x16x32_bf16 v[80:83], v[158:161], v[204:207], v[80:83]
	v_mfma_f32_16x16x32_bf16 v[76:79], v[132:135], v[212:215], v[76:79]
	v_mfma_f32_16x16x32_bf16 v[72:75], v[158:161], v[212:215], v[72:75]
	v_mfma_f32_16x16x32_bf16 v[68:71], v[132:135], v[220:223], v[68:71]
	v_mfma_f32_16x16x32_bf16 v[64:67], v[158:161], v[220:223], v[64:67]
	s_setprio 0
	s_setprio 1
	v_mfma_f32_16x16x32_bf16 v[28:31], v[162:165], v[192:195], v[28:31]
	v_mfma_f32_16x16x32_bf16 v[24:27], v[180:183], v[192:195], v[24:27]
	v_mfma_f32_16x16x32_bf16 v[20:23], v[162:165], v[200:203], v[20:23]
	v_mfma_f32_16x16x32_bf16 v[16:19], v[180:183], v[200:203], v[16:19]
	v_mfma_f32_16x16x32_bf16 v[12:15], v[162:165], v[208:211], v[12:15]
	v_mfma_f32_16x16x32_bf16 v[8:11], v[180:183], v[208:211], v[8:11]
	v_mfma_f32_16x16x32_bf16 v[4:7], v[162:165], v[216:219], v[4:7]
	v_mfma_f32_16x16x32_bf16 v[0:3], v[180:183], v[216:219], v[0:3]
	v_mfma_f32_16x16x32_bf16 v[28:31], v[176:179], v[196:199], v[28:31]
	v_mfma_f32_16x16x32_bf16 v[24:27], v[188:191], v[196:199], v[24:27]
	v_mfma_f32_16x16x32_bf16 v[20:23], v[176:179], v[204:207], v[20:23]
	v_mfma_f32_16x16x32_bf16 v[16:19], v[188:191], v[204:207], v[16:19]
	v_mfma_f32_16x16x32_bf16 v[12:15], v[176:179], v[212:215], v[12:15]
	v_mfma_f32_16x16x32_bf16 v[8:11], v[188:191], v[212:215], v[8:11]
	v_mfma_f32_16x16x32_bf16 v[4:7], v[176:179], v[220:223], v[4:7]
	v_mfma_f32_16x16x32_bf16 v[0:3], v[188:191], v[220:223], v[0:3]
	s_setprio 0
	s_barrier
	s_add_i32 s83, 0, 0x18000
	v_add_u32_e32 v148, s83, v169
	s_add_i32 s84, 0, 0x1c000
	ds_read_b128 v[128:131], v148
	ds_read_b128 v[132:135], v148 offset:1024
	ds_read_b128 v[154:157], v148 offset:2048
	ds_read_b128 v[158:161], v148 offset:3072
	v_add_u32_e32 v148, s84, v169
	ds_read_b128 v[162:165], v148
	ds_read_b128 v[176:179], v148 offset:1024
	ds_read_b128 v[180:183], v148 offset:2048
	ds_read_b128 v[188:191], v148 offset:3072
	s_mov_b32 m0, s71
	v_lshl_add_u64 v[228:229], s[60:61], 0, v[140:141]
	ds_read_b128 v[192:195], v174 offset:32768
	ds_read_b128 v[196:199], v174 offset:33792
	ds_read_b128 v[200:203], v174 offset:34816
	ds_read_b128 v[204:207], v174 offset:35840
	ds_read_b128 v[208:211], v174 offset:36864
	ds_read_b128 v[212:215], v174 offset:37888
	ds_read_b128 v[216:219], v174 offset:38912
	ds_read_b128 v[220:223], v174 offset:39936
	global_load_lds_dwordx4 v[228:229], off
	v_lshl_add_u64 v[228:229], s[60:61], 0, v[146:147]
	s_mov_b32 m0, s72
	s_nop 0
	global_load_lds_dwordx4 v[228:229], off
	s_waitcnt vmcnt(8)
	s_waitcnt lgkmcnt(0)
	s_barrier
	s_setprio 1
	s_waitcnt lgkmcnt(0)
	v_mfma_f32_16x16x32_bf16 v[124:127], v[128:131], v[192:195], v[124:127]
	v_mfma_f32_16x16x32_bf16 v[120:123], v[154:157], v[192:195], v[120:123]
	v_mfma_f32_16x16x32_bf16 v[116:119], v[128:131], v[200:203], v[116:119]
	v_mfma_f32_16x16x32_bf16 v[112:115], v[154:157], v[200:203], v[112:115]
	v_mfma_f32_16x16x32_bf16 v[108:111], v[128:131], v[208:211], v[108:111]
	v_mfma_f32_16x16x32_bf16 v[104:107], v[154:157], v[208:211], v[104:107]
	v_mfma_f32_16x16x32_bf16 v[100:103], v[128:131], v[216:219], v[100:103]
	v_mfma_f32_16x16x32_bf16 v[96:99], v[154:157], v[216:219], v[96:99]
	v_mfma_f32_16x16x32_bf16 v[124:127], v[132:135], v[196:199], v[124:127]
	v_mfma_f32_16x16x32_bf16 v[120:123], v[158:161], v[196:199], v[120:123]
	v_mfma_f32_16x16x32_bf16 v[116:119], v[132:135], v[204:207], v[116:119]
	v_mfma_f32_16x16x32_bf16 v[112:115], v[158:161], v[204:207], v[112:115]
	v_mfma_f32_16x16x32_bf16 v[108:111], v[132:135], v[212:215], v[108:111]
	v_mfma_f32_16x16x32_bf16 v[104:107], v[158:161], v[212:215], v[104:107]
	v_mfma_f32_16x16x32_bf16 v[100:103], v[132:135], v[220:223], v[100:103]
	v_mfma_f32_16x16x32_bf16 v[96:99], v[158:161], v[220:223], v[96:99]
	s_setprio 0
	s_setprio 1
	v_mfma_f32_16x16x32_bf16 v[60:63], v[162:165], v[192:195], v[60:63]
	v_mfma_f32_16x16x32_bf16 v[56:59], v[180:183], v[192:195], v[56:59]
	v_mfma_f32_16x16x32_bf16 v[52:55], v[162:165], v[200:203], v[52:55]
	v_mfma_f32_16x16x32_bf16 v[48:51], v[180:183], v[200:203], v[48:51]
	v_mfma_f32_16x16x32_bf16 v[44:47], v[162:165], v[208:211], v[44:47]
	v_mfma_f32_16x16x32_bf16 v[40:43], v[180:183], v[208:211], v[40:43]
	v_mfma_f32_16x16x32_bf16 v[36:39], v[162:165], v[216:219], v[36:39]
	v_mfma_f32_16x16x32_bf16 v[32:35], v[180:183], v[216:219], v[32:35]
	v_mfma_f32_16x16x32_bf16 v[60:63], v[176:179], v[196:199], v[60:63]
	v_mfma_f32_16x16x32_bf16 v[56:59], v[188:191], v[196:199], v[56:59]
	v_mfma_f32_16x16x32_bf16 v[52:55], v[176:179], v[204:207], v[52:55]
	v_mfma_f32_16x16x32_bf16 v[48:51], v[188:191], v[204:207], v[48:51]
	v_mfma_f32_16x16x32_bf16 v[44:47], v[176:179], v[212:215], v[44:47]
	v_mfma_f32_16x16x32_bf16 v[40:43], v[188:191], v[212:215], v[40:43]
	v_mfma_f32_16x16x32_bf16 v[36:39], v[176:179], v[220:223], v[36:39]
	v_mfma_f32_16x16x32_bf16 v[32:35], v[188:191], v[220:223], v[32:35]
	s_setprio 0
	s_barrier
	s_add_i32 s60, s83, s68
	v_lshl_add_u64 v[166:167], v[166:167], 0, s[18:19]
	s_mov_b32 m0, s60
	ds_read_b128 v[192:195], v174 offset:49152
	ds_read_b128 v[196:199], v174 offset:50176
	ds_read_b128 v[200:203], v174 offset:51200
	ds_read_b128 v[204:207], v174 offset:52224
	ds_read_b128 v[208:211], v174 offset:53248
	ds_read_b128 v[212:215], v174 offset:54272
	ds_read_b128 v[216:219], v174 offset:55296
	ds_read_b128 v[220:223], v174 offset:56320
	global_load_lds_dwordx4 v[166:167], off
	s_add_i32 m0, s60, 0x2000
	s_add_u32 s58, s58, 0x40080
	v_lshl_add_u64 v[166:167], v[184:185], 0, s[18:19]
	s_addc_u32 s59, s59, 0
	s_add_i32 s60, s84, s68
	global_load_lds_dwordx4 v[166:167], off
	v_lshl_add_u64 v[166:167], s[58:59], 0, v[136:137]
	s_mov_b32 m0, s60
	s_nop 0
	global_load_lds_dwordx4 v[166:167], off
	v_lshl_add_u64 v[166:167], s[58:59], 0, v[142:143]
	s_add_i32 m0, s60, 0x2000
	s_nop 0
	global_load_lds_dwordx4 v[166:167], off
	v_lshl_add_u64 v[166:167], v[224:225], 0, s[18:19]
	s_mov_b32 m0, s74
	s_nop 0
	global_load_lds_dwordx4 v[166:167], off
	v_lshl_add_u64 v[166:167], v[226:227], 0, s[18:19]
	s_mov_b32 m0, s75
	s_nop 0
	global_load_lds_dwordx4 v[166:167], off
	s_waitcnt vmcnt(8)
	s_waitcnt lgkmcnt(0)
	s_barrier
	s_setprio 1
	s_waitcnt lgkmcnt(0)
	v_mfma_f32_16x16x32_bf16 v[92:95], v[128:131], v[192:195], v[92:95]
	v_mfma_f32_16x16x32_bf16 v[88:91], v[154:157], v[192:195], v[88:91]
	v_mfma_f32_16x16x32_bf16 v[84:87], v[128:131], v[200:203], v[84:87]
	v_mfma_f32_16x16x32_bf16 v[80:83], v[154:157], v[200:203], v[80:83]
	v_mfma_f32_16x16x32_bf16 v[76:79], v[128:131], v[208:211], v[76:79]
	v_mfma_f32_16x16x32_bf16 v[72:75], v[154:157], v[208:211], v[72:75]
	v_mfma_f32_16x16x32_bf16 v[68:71], v[128:131], v[216:219], v[68:71]
	v_mfma_f32_16x16x32_bf16 v[64:67], v[154:157], v[216:219], v[64:67]
	v_mfma_f32_16x16x32_bf16 v[92:95], v[132:135], v[196:199], v[92:95]
	v_mfma_f32_16x16x32_bf16 v[88:91], v[158:161], v[196:199], v[88:91]
	v_mfma_f32_16x16x32_bf16 v[84:87], v[132:135], v[204:207], v[84:87]
	v_mfma_f32_16x16x32_bf16 v[80:83], v[158:161], v[204:207], v[80:83]
	v_mfma_f32_16x16x32_bf16 v[76:79], v[132:135], v[212:215], v[76:79]
	v_mfma_f32_16x16x32_bf16 v[72:75], v[158:161], v[212:215], v[72:75]
	v_mfma_f32_16x16x32_bf16 v[68:71], v[132:135], v[220:223], v[68:71]
	v_mfma_f32_16x16x32_bf16 v[64:67], v[158:161], v[220:223], v[64:67]
	s_setprio 0
	s_setprio 1
	v_mfma_f32_16x16x32_bf16 v[28:31], v[162:165], v[192:195], v[28:31]
	v_mfma_f32_16x16x32_bf16 v[24:27], v[180:183], v[192:195], v[24:27]
	v_mfma_f32_16x16x32_bf16 v[20:23], v[162:165], v[200:203], v[20:23]
	v_mfma_f32_16x16x32_bf16 v[16:19], v[180:183], v[200:203], v[16:19]
	v_mfma_f32_16x16x32_bf16 v[12:15], v[162:165], v[208:211], v[12:15]
	v_mfma_f32_16x16x32_bf16 v[8:11], v[180:183], v[208:211], v[8:11]
	v_mfma_f32_16x16x32_bf16 v[4:7], v[162:165], v[216:219], v[4:7]
	v_mfma_f32_16x16x32_bf16 v[0:3], v[180:183], v[216:219], v[0:3]
	v_mfma_f32_16x16x32_bf16 v[28:31], v[176:179], v[196:199], v[28:31]
	v_mfma_f32_16x16x32_bf16 v[24:27], v[188:191], v[196:199], v[24:27]
	v_mfma_f32_16x16x32_bf16 v[20:23], v[176:179], v[204:207], v[20:23]
	v_mfma_f32_16x16x32_bf16 v[16:19], v[188:191], v[204:207], v[16:19]
	v_mfma_f32_16x16x32_bf16 v[12:15], v[176:179], v[212:215], v[12:15]
	v_mfma_f32_16x16x32_bf16 v[8:11], v[188:191], v[212:215], v[8:11]
	v_mfma_f32_16x16x32_bf16 v[4:7], v[176:179], v[220:223], v[4:7]
	v_mfma_f32_16x16x32_bf16 v[0:3], v[188:191], v[220:223], v[0:3]
	s_add_i32 s82, s82, 2
	s_add_u32 s56, s56, 0x100
	s_addc_u32 s57, s57, 0
	s_add_u32 s80, s80, 0x100
	s_addc_u32 s81, s81, 0
	s_cmp_gt_u32 s82, 13
	s_setprio 0
	s_barrier
	s_cbranch_scc0 .LBB0_220
	s_and_b64 vcc, exec, s[20:21]
	s_cbranch_vccz .LBB0_223
	s_barrier

.Lp6kw_skip:
.Lp6kw_none:
	ds_read_b128 v[128:131], v165
	ds_read_b128 v[132:135], v165 offset:1024
	ds_read_b128 v[152:155], v165 offset:2048
	ds_read_b128 v[156:159], v165 offset:3072
	ds_read_b128 v[168:171], v166
	ds_read_b128 v[172:175], v166 offset:1024
	ds_read_b128 v[176:179], v166 offset:2048
	ds_read_b128 v[180:183], v166 offset:3072
	s_add_u32 s38, s36, 0x80
	s_addc_u32 s39, s37, 0
	s_cmp_eq_u32 s60, 12
	s_cselect_b32 s41, s21, s39
	s_cselect_b32 s40, s56, s38
	s_cselect_b32 s39, s23, s59
	s_cselect_b32 s38, s57, s58
	v_lshl_add_u64 v[160:161], s[36:37], 0, v[150:151]
	s_add_i32 m0, s46, 0xc000
	ds_read_b128 v[188:191], v167
	ds_read_b128 v[192:195], v167 offset:1024
	ds_read_b128 v[196:199], v167 offset:2048
	ds_read_b128 v[200:203], v167 offset:3072
	ds_read_b128 v[204:207], v167 offset:4096
	ds_read_b128 v[208:211], v167 offset:5120
	ds_read_b128 v[212:215], v167 offset:6144
	ds_read_b128 v[216:219], v167 offset:7168
	global_load_lds_dwordx4 v[160:161], off
	v_lshl_add_u64 v[160:161], s[36:37], 0, v[148:149]
	s_add_i32 m0, s46, 0xe000
	s_nop 0
	global_load_lds_dwordx4 v[160:161], off
	s_waitcnt vmcnt(8)
	s_waitcnt lgkmcnt(0)
	s_barrier
	s_setprio 1
	s_waitcnt lgkmcnt(0)
	v_mfma_f32_16x16x32_bf16 v[124:127], v[128:131], v[188:191], v[124:127]
	v_mfma_f32_16x16x32_bf16 v[120:123], v[152:155], v[188:191], v[120:123]
	v_mfma_f32_16x16x32_bf16 v[116:119], v[128:131], v[196:199], v[116:119]
	v_mfma_f32_16x16x32_bf16 v[112:115], v[152:155], v[196:199], v[112:115]
	v_mfma_f32_16x16x32_bf16 v[108:111], v[128:131], v[204:207], v[108:111]
	v_mfma_f32_16x16x32_bf16 v[104:107], v[152:155], v[204:207], v[104:107]
	v_mfma_f32_16x16x32_bf16 v[100:103], v[128:131], v[212:215], v[100:103]
	v_mfma_f32_16x16x32_bf16 v[96:99], v[152:155], v[212:215], v[96:99]
	v_mfma_f32_16x16x32_bf16 v[124:127], v[132:135], v[192:195], v[124:127]
	v_mfma_f32_16x16x32_bf16 v[120:123], v[156:159], v[192:195], v[120:123]
	v_mfma_f32_16x16x32_bf16 v[116:119], v[132:135], v[200:203], v[116:119]
	v_mfma_f32_16x16x32_bf16 v[112:115], v[156:159], v[200:203], v[112:115]
	v_mfma_f32_16x16x32_bf16 v[108:111], v[132:135], v[208:211], v[108:111]
	v_mfma_f32_16x16x32_bf16 v[104:107], v[156:159], v[208:211], v[104:107]
	v_mfma_f32_16x16x32_bf16 v[100:103], v[132:135], v[216:219], v[100:103]
	v_mfma_f32_16x16x32_bf16 v[96:99], v[156:159], v[216:219], v[96:99]
	s_setprio 0
	s_setprio 1
	v_mfma_f32_16x16x32_bf16 v[68:71], v[168:171], v[188:191], v[68:71]
	v_mfma_f32_16x16x32_bf16 v[64:67], v[176:179], v[188:191], v[64:67]
	v_mfma_f32_16x16x32_bf16 v[52:55], v[168:171], v[196:199], v[52:55]
	v_mfma_f32_16x16x32_bf16 v[48:51], v[176:179], v[196:199], v[48:51]
	v_mfma_f32_16x16x32_bf16 v[44:47], v[168:171], v[204:207], v[44:47]
	v_mfma_f32_16x16x32_bf16 v[40:43], v[176:179], v[204:207], v[40:43]
	v_mfma_f32_16x16x32_bf16 v[36:39], v[168:171], v[212:215], v[36:39]
	v_mfma_f32_16x16x32_bf16 v[32:35], v[176:179], v[212:215], v[32:35]
	v_mfma_f32_16x16x32_bf16 v[68:71], v[172:175], v[192:195], v[68:71]
	v_mfma_f32_16x16x32_bf16 v[64:67], v[180:183], v[192:195], v[64:67]
	v_mfma_f32_16x16x32_bf16 v[52:55], v[172:175], v[200:203], v[52:55]
	v_mfma_f32_16x16x32_bf16 v[48:51], v[180:183], v[200:203], v[48:51]
	v_mfma_f32_16x16x32_bf16 v[44:47], v[172:175], v[208:211], v[44:47]
	v_mfma_f32_16x16x32_bf16 v[40:43], v[180:183], v[208:211], v[40:43]
	v_mfma_f32_16x16x32_bf16 v[36:39], v[172:175], v[216:219], v[36:39]
	v_mfma_f32_16x16x32_bf16 v[32:35], v[180:183], v[216:219], v[32:35]
	s_setprio 0
	s_barrier
	s_add_i32 s61, s54, s45
	v_lshl_add_u64 v[160:161], s[38:39], 0, v[146:147]
	s_mov_b32 m0, s61
	ds_read_b128 v[188:191], v167 offset:16384
	ds_read_b128 v[192:195], v167 offset:17408
	ds_read_b128 v[196:199], v167 offset:18432
	ds_read_b128 v[200:203], v167 offset:19456
	ds_read_b128 v[204:207], v167 offset:20480
	ds_read_b128 v[208:211], v167 offset:21504
	ds_read_b128 v[212:215], v167 offset:22528
	ds_read_b128 v[216:219], v167 offset:23552
	global_load_lds_dwordx4 v[160:161], off
	s_add_i32 m0, s61, 0x2000
	s_add_u32 s62, s38, 0x40000
	v_lshl_add_u64 v[184:185], s[38:39], 0, v[140:141]
	s_addc_u32 s63, s39, 0
	s_add_i32 s61, s55, s45
	global_load_lds_dwordx4 v[184:185], off
	v_lshl_add_u64 v[220:221], s[62:63], 0, v[146:147]
	s_mov_b32 m0, s61
	v_lshl_add_u64 v[222:223], s[40:41], 0, v[136:137]
	global_load_lds_dwordx4 v[220:221], off
	v_lshl_add_u64 v[220:221], s[62:63], 0, v[140:141]
	s_add_i32 m0, s61, 0x2000
	s_nop 0
	global_load_lds_dwordx4 v[220:221], off
	v_lshl_add_u64 v[220:221], s[40:41], 0, v[142:143]
	s_mov_b32 m0, s46
	s_nop 0
	global_load_lds_dwordx4 v[220:221], off
	s_mov_b32 m0, s47
	s_nop 0
	global_load_lds_dwordx4 v[222:223], off
	s_waitcnt vmcnt(8)
	s_waitcnt lgkmcnt(0)
	s_barrier
	s_setprio 1
	s_waitcnt lgkmcnt(0)
	v_mfma_f32_16x16x32_bf16 v[92:95], v[128:131], v[188:191], v[92:95]
	v_mfma_f32_16x16x32_bf16 v[88:91], v[152:155], v[188:191], v[88:91]
	v_mfma_f32_16x16x32_bf16 v[84:87], v[128:131], v[196:199], v[84:87]
	v_mfma_f32_16x16x32_bf16 v[80:83], v[152:155], v[196:199], v[80:83]
	v_mfma_f32_16x16x32_bf16 v[76:79], v[128:131], v[204:207], v[76:79]
	v_mfma_f32_16x16x32_bf16 v[72:75], v[152:155], v[204:207], v[72:75]
	v_mfma_f32_16x16x32_bf16 v[60:63], v[128:131], v[212:215], v[60:63]
	v_mfma_f32_16x16x32_bf16 v[56:59], v[152:155], v[212:215], v[56:59]
	v_mfma_f32_16x16x32_bf16 v[92:95], v[132:135], v[192:195], v[92:95]
	v_mfma_f32_16x16x32_bf16 v[88:91], v[156:159], v[192:195], v[88:91]
	v_mfma_f32_16x16x32_bf16 v[84:87], v[132:135], v[200:203], v[84:87]
	v_mfma_f32_16x16x32_bf16 v[80:83], v[156:159], v[200:203], v[80:83]
	v_mfma_f32_16x16x32_bf16 v[76:79], v[132:135], v[208:211], v[76:79]
	v_mfma_f32_16x16x32_bf16 v[72:75], v[156:159], v[208:211], v[72:75]
	v_mfma_f32_16x16x32_bf16 v[60:63], v[132:135], v[216:219], v[60:63]
	v_mfma_f32_16x16x32_bf16 v[56:59], v[156:159], v[216:219], v[56:59]
	s_setprio 0
	s_setprio 1
	v_mfma_f32_16x16x32_bf16 v[28:31], v[168:171], v[188:191], v[28:31]
	v_mfma_f32_16x16x32_bf16 v[24:27], v[176:179], v[188:191], v[24:27]
	v_mfma_f32_16x16x32_bf16 v[20:23], v[168:171], v[196:199], v[20:23]
	v_mfma_f32_16x16x32_bf16 v[16:19], v[176:179], v[196:199], v[16:19]
	v_mfma_f32_16x16x32_bf16 v[12:15], v[168:171], v[204:207], v[12:15]
	v_mfma_f32_16x16x32_bf16 v[8:11], v[176:179], v[204:207], v[8:11]
	v_mfma_f32_16x16x32_bf16 v[4:7], v[168:171], v[212:215], v[4:7]
	v_mfma_f32_16x16x32_bf16 v[0:3], v[176:179], v[212:215], v[0:3]
	v_mfma_f32_16x16x32_bf16 v[28:31], v[172:175], v[192:195], v[28:31]
	v_mfma_f32_16x16x32_bf16 v[24:27], v[180:183], v[192:195], v[24:27]
	v_mfma_f32_16x16x32_bf16 v[20:23], v[172:175], v[200:203], v[20:23]
	v_mfma_f32_16x16x32_bf16 v[16:19], v[180:183], v[200:203], v[16:19]
	v_mfma_f32_16x16x32_bf16 v[12:15], v[172:175], v[208:211], v[12:15]
	v_mfma_f32_16x16x32_bf16 v[8:11], v[180:183], v[208:211], v[8:11]
	v_mfma_f32_16x16x32_bf16 v[4:7], v[172:175], v[216:219], v[4:7]
	v_mfma_f32_16x16x32_bf16 v[0:3], v[180:183], v[216:219], v[0:3]
	s_setprio 0
	s_barrier
	s_add_i32 s61, 0, 0x18000
	s_add_i32 s62, 0, 0x1c000
	v_add_u32_e32 v156, s61, v163
	v_add_u32_e32 v180, s62, v163
	ds_read_b128 v[128:131], v156
	ds_read_b128 v[132:135], v156 offset:1024
	ds_read_b128 v[152:155], v156 offset:2048
	ds_read_b128 v[156:159], v156 offset:3072
	ds_read_b128 v[168:171], v180
	ds_read_b128 v[172:175], v180 offset:1024
	ds_read_b128 v[176:179], v180 offset:2048
	ds_read_b128 v[180:183], v180 offset:3072
	s_mov_b32 m0, s48
	v_lshl_add_u64 v[224:225], s[40:41], 0, v[144:145]
	ds_read_b128 v[188:191], v167 offset:32768
	ds_read_b128 v[192:195], v167 offset:33792
	ds_read_b128 v[196:199], v167 offset:34816
	ds_read_b128 v[200:203], v167 offset:35840
	ds_read_b128 v[204:207], v167 offset:36864
	ds_read_b128 v[208:211], v167 offset:37888
	ds_read_b128 v[212:215], v167 offset:38912
	ds_read_b128 v[216:219], v167 offset:39936
	global_load_lds_dwordx4 v[224:225], off
	v_lshl_add_u64 v[224:225], s[40:41], 0, v[138:139]
	s_mov_b32 m0, s49
	s_nop 0
	global_load_lds_dwordx4 v[224:225], off
	s_waitcnt vmcnt(8)
	s_waitcnt lgkmcnt(0)
	s_barrier
	s_setprio 1
	s_waitcnt lgkmcnt(0)
	v_mfma_f32_16x16x32_bf16 v[124:127], v[128:131], v[188:191], v[124:127]
	v_mfma_f32_16x16x32_bf16 v[120:123], v[152:155], v[188:191], v[120:123]
	v_mfma_f32_16x16x32_bf16 v[116:119], v[128:131], v[196:199], v[116:119]
	v_mfma_f32_16x16x32_bf16 v[112:115], v[152:155], v[196:199], v[112:115]
	v_mfma_f32_16x16x32_bf16 v[108:111], v[128:131], v[204:207], v[108:111]
	v_mfma_f32_16x16x32_bf16 v[104:107], v[152:155], v[204:207], v[104:107]
	v_mfma_f32_16x16x32_bf16 v[100:103], v[128:131], v[212:215], v[100:103]
	v_mfma_f32_16x16x32_bf16 v[96:99], v[152:155], v[212:215], v[96:99]
	v_mfma_f32_16x16x32_bf16 v[124:127], v[132:135], v[192:195], v[124:127]
	v_mfma_f32_16x16x32_bf16 v[120:123], v[156:159], v[192:195], v[120:123]
	v_mfma_f32_16x16x32_bf16 v[116:119], v[132:135], v[200:203], v[116:119]
	v_mfma_f32_16x16x32_bf16 v[112:115], v[156:159], v[200:203], v[112:115]
	v_mfma_f32_16x16x32_bf16 v[108:111], v[132:135], v[208:211], v[108:111]
	v_mfma_f32_16x16x32_bf16 v[104:107], v[156:159], v[208:211], v[104:107]
	v_mfma_f32_16x16x32_bf16 v[100:103], v[132:135], v[216:219], v[100:103]
	v_mfma_f32_16x16x32_bf16 v[96:99], v[156:159], v[216:219], v[96:99]
	s_setprio 0
	s_setprio 1
	v_mfma_f32_16x16x32_bf16 v[68:71], v[168:171], v[188:191], v[68:71]
	v_mfma_f32_16x16x32_bf16 v[64:67], v[176:179], v[188:191], v[64:67]
	v_mfma_f32_16x16x32_bf16 v[52:55], v[168:171], v[196:199], v[52:55]
	v_mfma_f32_16x16x32_bf16 v[48:51], v[176:179], v[196:199], v[48:51]
	v_mfma_f32_16x16x32_bf16 v[44:47], v[168:171], v[204:207], v[44:47]
	v_mfma_f32_16x16x32_bf16 v[40:43], v[176:179], v[204:207], v[40:43]
	v_mfma_f32_16x16x32_bf16 v[36:39], v[168:171], v[212:215], v[36:39]
	v_mfma_f32_16x16x32_bf16 v[32:35], v[176:179], v[212:215], v[32:35]
	v_mfma_f32_16x16x32_bf16 v[68:71], v[172:175], v[192:195], v[68:71]
	v_mfma_f32_16x16x32_bf16 v[64:67], v[180:183], v[192:195], v[64:67]
	v_mfma_f32_16x16x32_bf16 v[52:55], v[172:175], v[200:203], v[52:55]
	v_mfma_f32_16x16x32_bf16 v[48:51], v[180:183], v[200:203], v[48:51]
	v_mfma_f32_16x16x32_bf16 v[44:47], v[172:175], v[208:211], v[44:47]
	v_mfma_f32_16x16x32_bf16 v[40:43], v[180:183], v[208:211], v[40:43]
	v_mfma_f32_16x16x32_bf16 v[36:39], v[172:175], v[216:219], v[36:39]
	v_mfma_f32_16x16x32_bf16 v[32:35], v[180:183], v[216:219], v[32:35]
	s_setprio 0
	s_barrier
	s_add_i32 s40, s61, s45
	v_lshl_add_u64 v[160:161], v[160:161], 0, s[8:9]
	s_mov_b32 m0, s40
	ds_read_b128 v[188:191], v167 offset:49152
	ds_read_b128 v[192:195], v167 offset:50176
	ds_read_b128 v[196:199], v167 offset:51200
	ds_read_b128 v[200:203], v167 offset:52224
	ds_read_b128 v[204:207], v167 offset:53248
	ds_read_b128 v[208:211], v167 offset:54272
	ds_read_b128 v[212:215], v167 offset:55296
	ds_read_b128 v[216:219], v167 offset:56320
	global_load_lds_dwordx4 v[160:161], off
	s_add_i32 m0, s40, 0x2000
	s_add_u32 s38, s38, 0x40080
	v_lshl_add_u64 v[160:161], v[184:185], 0, s[8:9]
	s_addc_u32 s39, s39, 0
	s_add_i32 s40, s62, s45
	global_load_lds_dwordx4 v[160:161], off
	v_lshl_add_u64 v[160:161], s[38:39], 0, v[146:147]
	s_mov_b32 m0, s40
	s_nop 0
	global_load_lds_dwordx4 v[160:161], off
	v_lshl_add_u64 v[160:161], s[38:39], 0, v[140:141]
	s_add_i32 m0, s40, 0x2000
	s_nop 0
	global_load_lds_dwordx4 v[160:161], off
	v_lshl_add_u64 v[160:161], v[220:221], 0, s[8:9]
	s_mov_b32 m0, s51
	s_nop 0
	global_load_lds_dwordx4 v[160:161], off
	v_lshl_add_u64 v[160:161], v[222:223], 0, s[8:9]
	s_mov_b32 m0, s53
	s_nop 0
	global_load_lds_dwordx4 v[160:161], off
	s_waitcnt vmcnt(8)
	s_waitcnt lgkmcnt(0)
	s_barrier
	s_setprio 1
	s_waitcnt lgkmcnt(0)
	v_mfma_f32_16x16x32_bf16 v[92:95], v[128:131], v[188:191], v[92:95]
	v_mfma_f32_16x16x32_bf16 v[88:91], v[152:155], v[188:191], v[88:91]
	v_mfma_f32_16x16x32_bf16 v[84:87], v[128:131], v[196:199], v[84:87]
	v_mfma_f32_16x16x32_bf16 v[80:83], v[152:155], v[196:199], v[80:83]
	v_mfma_f32_16x16x32_bf16 v[76:79], v[128:131], v[204:207], v[76:79]
	v_mfma_f32_16x16x32_bf16 v[72:75], v[152:155], v[204:207], v[72:75]
	v_mfma_f32_16x16x32_bf16 v[60:63], v[128:131], v[212:215], v[60:63]
	v_mfma_f32_16x16x32_bf16 v[56:59], v[152:155], v[212:215], v[56:59]
	v_mfma_f32_16x16x32_bf16 v[92:95], v[132:135], v[192:195], v[92:95]
	v_mfma_f32_16x16x32_bf16 v[88:91], v[156:159], v[192:195], v[88:91]
	v_mfma_f32_16x16x32_bf16 v[84:87], v[132:135], v[200:203], v[84:87]
	v_mfma_f32_16x16x32_bf16 v[80:83], v[156:159], v[200:203], v[80:83]
	v_mfma_f32_16x16x32_bf16 v[76:79], v[132:135], v[208:211], v[76:79]
	v_mfma_f32_16x16x32_bf16 v[72:75], v[156:159], v[208:211], v[72:75]
	v_mfma_f32_16x16x32_bf16 v[60:63], v[132:135], v[216:219], v[60:63]
	v_mfma_f32_16x16x32_bf16 v[56:59], v[156:159], v[216:219], v[56:59]
	s_setprio 0
	s_setprio 1
	v_mfma_f32_16x16x32_bf16 v[28:31], v[168:171], v[188:191], v[28:31]
	v_mfma_f32_16x16x32_bf16 v[24:27], v[176:179], v[188:191], v[24:27]
	v_mfma_f32_16x16x32_bf16 v[20:23], v[168:171], v[196:199], v[20:23]
	v_mfma_f32_16x16x32_bf16 v[16:19], v[176:179], v[196:199], v[16:19]
	v_mfma_f32_16x16x32_bf16 v[12:15], v[168:171], v[204:207], v[12:15]
	v_mfma_f32_16x16x32_bf16 v[8:11], v[176:179], v[204:207], v[8:11]
	v_mfma_f32_16x16x32_bf16 v[4:7], v[168:171], v[212:215], v[4:7]
	v_mfma_f32_16x16x32_bf16 v[0:3], v[176:179], v[212:215], v[0:3]
	v_mfma_f32_16x16x32_bf16 v[28:31], v[172:175], v[192:195], v[28:31]
	v_mfma_f32_16x16x32_bf16 v[24:27], v[180:183], v[192:195], v[24:27]
	v_mfma_f32_16x16x32_bf16 v[20:23], v[172:175], v[200:203], v[20:23]
	v_mfma_f32_16x16x32_bf16 v[16:19], v[180:183], v[200:203], v[16:19]
	v_mfma_f32_16x16x32_bf16 v[12:15], v[172:175], v[208:211], v[12:15]
	v_mfma_f32_16x16x32_bf16 v[8:11], v[180:183], v[208:211], v[8:11]
	v_mfma_f32_16x16x32_bf16 v[4:7], v[172:175], v[216:219], v[4:7]
	v_mfma_f32_16x16x32_bf16 v[0:3], v[180:183], v[216:219], v[0:3]
	s_add_i32 s60, s60, 2
	s_add_u32 s36, s36, 0x100
	s_addc_u32 s37, s37, 0
	s_add_u32 s58, s58, 0x100
	s_addc_u32 s59, s59, 0
	s_cmp_gt_u32 s60, 13
	s_setprio 0
	s_barrier
	s_cbranch_scc0 .LBB0_566
	s_and_b64 vcc, exec, s[10:11]
	s_cbranch_vccz .LBB0_569
	s_barrier

.LBB0_1106:
	s_add_u32 s34, s24, s30
	v_add_u32_e32 v0, s45, v192
	v_add_u32_e32 v12, s48, v192
	s_addc_u32 s35, s25, s31
	ds_read_b128 v[16:19], v0
	ds_read_b128 v[20:23], v0 offset:1024
	ds_read_b128 v[24:27], v0 offset:2048
	ds_read_b128 v[28:31], v0 offset:3072
	ds_read_b128 v[0:3], v12
	ds_read_b128 v[4:7], v12 offset:1024
	ds_read_b128 v[8:11], v12 offset:2048
	ds_read_b128 v[12:15], v12 offset:3072
	s_add_u32 s36, s34, 0xe173100
	s_addc_u32 s37, s35, 0
	s_and_b64 s[34:35], s[0:1], exec
	s_cselect_b32 s37, s3, s37
	s_cselect_b32 s36, s2, s36
	s_add_u32 s61, s58, s30
	s_addc_u32 s62, s59, s31
	s_and_b64 s[34:35], s[0:1], exec
	s_cselect_b32 s35, s19, s62
	s_cselect_b32 s34, s57, s61
	v_cndmask_b32_e64 v160, v198, v167, s[0:1]
	v_cndmask_b32_e64 v201, v166, v169, s[0:1]
	v_cndmask_b32_e64 v180, v170, v196, s[0:1]
	v_cndmask_b32_e64 v234, v168, v197, s[0:1]
	s_mov_b32 m0, s50
	v_lshl_add_u64 v[176:177], v[174:175], 0, s[30:31]
	ds_read_b128 v[202:205], v194
	ds_read_b128 v[206:209], v194 offset:1024
	ds_read_b128 v[210:213], v194 offset:2048
	ds_read_b128 v[214:217], v194 offset:3072
	ds_read_b128 v[218:221], v194 offset:4096
	ds_read_b128 v[222:225], v194 offset:5120
	ds_read_b128 v[226:229], v194 offset:6144
	ds_read_b128 v[230:233], v194 offset:7168
	global_load_lds_dwordx4 v[176:177], off
	v_lshl_add_u64 v[176:177], v[172:173], 0, s[30:31]
	s_mov_b32 m0, s51
	s_nop 0
	global_load_lds_dwordx4 v[176:177], off
	s_waitcnt vmcnt(8)
	s_waitcnt lgkmcnt(0)
	s_barrier
	s_setprio 1
	s_waitcnt lgkmcnt(0)
	v_mfma_scale_f32_16x16x128_f8f6f4 v[156:159], v[16:23], v[202:209], v[156:159], v190, v191 op_sel_hi:[0,0,0]
	v_mfma_scale_f32_16x16x128_f8f6f4 v[148:151], v[24:31], v[202:209], v[148:151], v190, v191 op_sel_hi:[0,0,0]
	v_mfma_scale_f32_16x16x128_f8f6f4 v[140:143], v[16:23], v[210:217], v[140:143], v190, v191 op_sel_hi:[0,0,0]
	v_mfma_scale_f32_16x16x128_f8f6f4 v[132:135], v[24:31], v[210:217], v[132:135], v190, v191 op_sel_hi:[0,0,0]
	v_mfma_scale_f32_16x16x128_f8f6f4 v[124:127], v[16:23], v[218:225], v[124:127], v190, v191 op_sel_hi:[0,0,0]
	v_mfma_scale_f32_16x16x128_f8f6f4 v[116:119], v[24:31], v[218:225], v[116:119], v190, v191 op_sel_hi:[0,0,0]
	v_mfma_scale_f32_16x16x128_f8f6f4 v[108:111], v[16:23], v[226:233], v[108:111], v190, v191 op_sel_hi:[0,0,0]
	v_mfma_scale_f32_16x16x128_f8f6f4 v[100:103], v[24:31], v[226:233], v[100:103], v190, v191 op_sel_hi:[0,0,0]
	s_setprio 0
	s_setprio 1
	v_mfma_scale_f32_16x16x128_f8f6f4 v[152:155], v[0:7], v[202:209], v[152:155], v190, v191 op_sel_hi:[0,0,0]
	v_mfma_scale_f32_16x16x128_f8f6f4 v[144:147], v[8:15], v[202:209], v[144:147], v190, v191 op_sel_hi:[0,0,0]
	v_mfma_scale_f32_16x16x128_f8f6f4 v[136:139], v[0:7], v[210:217], v[136:139], v190, v191 op_sel_hi:[0,0,0]
	v_mfma_scale_f32_16x16x128_f8f6f4 v[128:131], v[8:15], v[210:217], v[128:131], v190, v191 op_sel_hi:[0,0,0]
	v_mfma_scale_f32_16x16x128_f8f6f4 v[120:123], v[0:7], v[218:225], v[120:123], v190, v191 op_sel_hi:[0,0,0]
	v_mfma_scale_f32_16x16x128_f8f6f4 v[112:115], v[8:15], v[218:225], v[112:115], v190, v191 op_sel_hi:[0,0,0]
	v_mfma_scale_f32_16x16x128_f8f6f4 v[104:107], v[0:7], v[226:233], v[104:107], v190, v191 op_sel_hi:[0,0,0]
	v_mfma_scale_f32_16x16x128_f8f6f4 v[96:99], v[8:15], v[226:233], v[96:99], v190, v191 op_sel_hi:[0,0,0]
	s_setprio 0
	s_barrier
	s_mov_b32 m0, s52
	v_lshl_add_u64 v[178:179], s[34:35], 0, v[164:165]
	s_add_u32 s0, s34, 0x20000
	ds_read_b128 v[202:205], v194 offset:16384
	ds_read_b128 v[206:209], v194 offset:17408
	ds_read_b128 v[210:213], v194 offset:18432
	ds_read_b128 v[214:217], v194 offset:19456
	ds_read_b128 v[218:221], v194 offset:20480
	ds_read_b128 v[222:225], v194 offset:21504
	ds_read_b128 v[226:229], v194 offset:22528
	ds_read_b128 v[230:233], v194 offset:23552
	global_load_lds_dwordx4 v[178:179], off
	v_lshl_add_u64 v[176:177], s[34:35], 0, v[162:163]
	s_mov_b32 m0, s53
	s_addc_u32 s1, s35, 0
	global_load_lds_dwordx4 v[176:177], off
	v_lshl_add_u64 v[182:183], s[0:1], 0, v[164:165]
	s_mov_b32 m0, s54
	v_mov_b32_e32 v181, v161
	global_load_lds_dwordx4 v[182:183], off
	v_lshl_add_u64 v[182:183], s[0:1], 0, v[162:163]
	s_mov_b32 m0, s55
	s_nop 0
	global_load_lds_dwordx4 v[182:183], off
	s_mov_b32 m0, s27
	v_lshl_add_u64 v[182:183], s[36:37], 0, v[160:161]
	global_load_lds_dwordx4 v160, s[36:37]
	s_mov_b32 m0, s38
	s_nop 0
	global_load_lds_dwordx4 v180, s[36:37]
	s_waitcnt vmcnt(8)
	s_waitcnt lgkmcnt(0)
	v_lshl_add_u64 v[180:181], s[36:37], 0, v[180:181]
	s_barrier
	s_setprio 1
	s_waitcnt lgkmcnt(0)
	v_mfma_scale_f32_16x16x128_f8f6f4 v[92:95], v[16:23], v[202:209], v[92:95], v190, v191 op_sel_hi:[0,0,0]
	v_mfma_scale_f32_16x16x128_f8f6f4 v[84:87], v[24:31], v[202:209], v[84:87], v190, v191 op_sel_hi:[0,0,0]
	v_mfma_scale_f32_16x16x128_f8f6f4 v[76:79], v[16:23], v[210:217], v[76:79], v190, v191 op_sel_hi:[0,0,0]
	v_mfma_scale_f32_16x16x128_f8f6f4 v[68:71], v[24:31], v[210:217], v[68:71], v190, v191 op_sel_hi:[0,0,0]
	v_mfma_scale_f32_16x16x128_f8f6f4 v[60:63], v[16:23], v[218:225], v[60:63], v190, v191 op_sel_hi:[0,0,0]
	v_mfma_scale_f32_16x16x128_f8f6f4 v[52:55], v[24:31], v[218:225], v[52:55], v190, v191 op_sel_hi:[0,0,0]
	v_mfma_scale_f32_16x16x128_f8f6f4 v[44:47], v[16:23], v[226:233], v[44:47], v190, v191 op_sel_hi:[0,0,0]
	v_mfma_scale_f32_16x16x128_f8f6f4 v[36:39], v[24:31], v[226:233], v[36:39], v190, v191 op_sel_hi:[0,0,0]
	s_setprio 0
	s_setprio 1
	v_mfma_scale_f32_16x16x128_f8f6f4 v[88:91], v[0:7], v[202:209], v[88:91], v190, v191 op_sel_hi:[0,0,0]
	v_mfma_scale_f32_16x16x128_f8f6f4 v[80:83], v[8:15], v[202:209], v[80:83], v190, v191 op_sel_hi:[0,0,0]
	v_mfma_scale_f32_16x16x128_f8f6f4 v[72:75], v[0:7], v[210:217], v[72:75], v190, v191 op_sel_hi:[0,0,0]
	v_mfma_scale_f32_16x16x128_f8f6f4 v[64:67], v[8:15], v[210:217], v[64:67], v190, v191 op_sel_hi:[0,0,0]
	v_mfma_scale_f32_16x16x128_f8f6f4 v[56:59], v[0:7], v[218:225], v[56:59], v190, v191 op_sel_hi:[0,0,0]
	v_mfma_scale_f32_16x16x128_f8f6f4 v[48:51], v[8:15], v[218:225], v[48:51], v190, v191 op_sel_hi:[0,0,0]
	v_mfma_scale_f32_16x16x128_f8f6f4 v[40:43], v[0:7], v[226:233], v[40:43], v190, v191 op_sel_hi:[0,0,0]
	v_mfma_scale_f32_16x16x128_f8f6f4 v[32:35], v[8:15], v[226:233], v[32:35], v190, v191 op_sel_hi:[0,0,0]
	s_setprio 0
	s_barrier
	s_add_i32 s0, 0, 0x18000
	s_add_i32 s1, 0, 0x1c000
	v_add_u32_e32 v0, s0, v192
	v_add_u32_e32 v12, s1, v192
	ds_read_b128 v[16:19], v0
	ds_read_b128 v[20:23], v0 offset:1024
	ds_read_b128 v[24:27], v0 offset:2048
	ds_read_b128 v[28:31], v0 offset:3072
	ds_read_b128 v[0:3], v12
	ds_read_b128 v[4:7], v12 offset:1024
	ds_read_b128 v[8:11], v12 offset:2048
	ds_read_b128 v[12:15], v12 offset:3072
	s_mov_b32 m0, s39
	ds_read_b128 v[202:205], v194 offset:32768
	ds_read_b128 v[206:209], v194 offset:33792
	ds_read_b128 v[210:213], v194 offset:34816
	ds_read_b128 v[214:217], v194 offset:35840
	ds_read_b128 v[218:221], v194 offset:36864
	ds_read_b128 v[222:225], v194 offset:37888
	ds_read_b128 v[226:229], v194 offset:38912
	ds_read_b128 v[230:233], v194 offset:39936
	global_load_lds_dwordx4 v201, s[36:37]
	s_mov_b32 m0, s40
	s_nop 0
	global_load_lds_dwordx4 v234, s[36:37]
	s_waitcnt vmcnt(8)
	s_waitcnt lgkmcnt(0)
	s_barrier
	s_setprio 1
	s_waitcnt lgkmcnt(0)
	v_mfma_scale_f32_16x16x128_f8f6f4 v[156:159], v[16:23], v[202:209], v[156:159], v190, v191 op_sel_hi:[0,0,0]
	v_mfma_scale_f32_16x16x128_f8f6f4 v[148:151], v[24:31], v[202:209], v[148:151], v190, v191 op_sel_hi:[0,0,0]
	v_mfma_scale_f32_16x16x128_f8f6f4 v[140:143], v[16:23], v[210:217], v[140:143], v190, v191 op_sel_hi:[0,0,0]
	v_mfma_scale_f32_16x16x128_f8f6f4 v[132:135], v[24:31], v[210:217], v[132:135], v190, v191 op_sel_hi:[0,0,0]
	v_mfma_scale_f32_16x16x128_f8f6f4 v[124:127], v[16:23], v[218:225], v[124:127], v190, v191 op_sel_hi:[0,0,0]
	v_mfma_scale_f32_16x16x128_f8f6f4 v[116:119], v[24:31], v[218:225], v[116:119], v190, v191 op_sel_hi:[0,0,0]
	v_mfma_scale_f32_16x16x128_f8f6f4 v[108:111], v[16:23], v[226:233], v[108:111], v190, v191 op_sel_hi:[0,0,0]
	v_mfma_scale_f32_16x16x128_f8f6f4 v[100:103], v[24:31], v[226:233], v[100:103], v190, v191 op_sel_hi:[0,0,0]
	s_setprio 0
	s_setprio 1
	v_mfma_scale_f32_16x16x128_f8f6f4 v[152:155], v[0:7], v[202:209], v[152:155], v190, v191 op_sel_hi:[0,0,0]
	v_mfma_scale_f32_16x16x128_f8f6f4 v[144:147], v[8:15], v[202:209], v[144:147], v190, v191 op_sel_hi:[0,0,0]
	v_mfma_scale_f32_16x16x128_f8f6f4 v[136:139], v[0:7], v[210:217], v[136:139], v190, v191 op_sel_hi:[0,0,0]
	v_mfma_scale_f32_16x16x128_f8f6f4 v[128:131], v[8:15], v[210:217], v[128:131], v190, v191 op_sel_hi:[0,0,0]
	v_mfma_scale_f32_16x16x128_f8f6f4 v[120:123], v[0:7], v[218:225], v[120:123], v190, v191 op_sel_hi:[0,0,0]
	v_mfma_scale_f32_16x16x128_f8f6f4 v[112:115], v[8:15], v[218:225], v[112:115], v190, v191 op_sel_hi:[0,0,0]
	v_mfma_scale_f32_16x16x128_f8f6f4 v[104:107], v[0:7], v[226:233], v[104:107], v190, v191 op_sel_hi:[0,0,0]
	v_mfma_scale_f32_16x16x128_f8f6f4 v[96:99], v[8:15], v[226:233], v[96:99], v190, v191 op_sel_hi:[0,0,0]
	s_setprio 0
	s_barrier
	s_add_i32 s0, s0, s23
	v_lshl_add_u64 v[178:179], v[178:179], 0, s[8:9]
	s_mov_b32 m0, s0
	ds_read_b128 v[202:205], v194 offset:49152
	ds_read_b128 v[206:209], v194 offset:50176
	ds_read_b128 v[210:213], v194 offset:51200
	ds_read_b128 v[214:217], v194 offset:52224
	ds_read_b128 v[218:221], v194 offset:53248
	ds_read_b128 v[222:225], v194 offset:54272
	ds_read_b128 v[226:229], v194 offset:55296
	ds_read_b128 v[230:233], v194 offset:56320
	global_load_lds_dwordx4 v[178:179], off
	s_add_i32 m0, s0, 0x2000
	s_add_u32 s34, s34, 0x20080
	v_lshl_add_u64 v[176:177], v[176:177], 0, s[8:9]
	s_addc_u32 s35, s35, 0
	s_add_i32 s0, s1, s23
	global_load_lds_dwordx4 v[176:177], off
	v_lshl_add_u64 v[176:177], s[34:35], 0, v[164:165]
	s_mov_b32 m0, s0
	s_nop 0
	global_load_lds_dwordx4 v[176:177], off
	v_lshl_add_u64 v[176:177], s[34:35], 0, v[162:163]
	s_add_i32 m0, s0, 0x2000
	s_nop 0
	global_load_lds_dwordx4 v[176:177], off
	v_lshl_add_u64 v[176:177], v[182:183], 0, s[8:9]
	s_mov_b32 m0, s42
	s_nop 0
	global_load_lds_dwordx4 v[176:177], off
	v_lshl_add_u64 v[176:177], v[180:181], 0, s[8:9]
	s_mov_b32 m0, s43
	s_nop 0
	global_load_lds_dwordx4 v[176:177], off
	s_waitcnt vmcnt(8)
	s_waitcnt lgkmcnt(0)
	s_barrier
	s_setprio 1
	s_waitcnt lgkmcnt(0)
	v_mfma_scale_f32_16x16x128_f8f6f4 v[92:95], v[16:23], v[202:209], v[92:95], v190, v191 op_sel_hi:[0,0,0]
	v_mfma_scale_f32_16x16x128_f8f6f4 v[84:87], v[24:31], v[202:209], v[84:87], v190, v191 op_sel_hi:[0,0,0]
	v_mfma_scale_f32_16x16x128_f8f6f4 v[76:79], v[16:23], v[210:217], v[76:79], v190, v191 op_sel_hi:[0,0,0]
	v_mfma_scale_f32_16x16x128_f8f6f4 v[68:71], v[24:31], v[210:217], v[68:71], v190, v191 op_sel_hi:[0,0,0]
	v_mfma_scale_f32_16x16x128_f8f6f4 v[60:63], v[16:23], v[218:225], v[60:63], v190, v191 op_sel_hi:[0,0,0]
	v_mfma_scale_f32_16x16x128_f8f6f4 v[52:55], v[24:31], v[218:225], v[52:55], v190, v191 op_sel_hi:[0,0,0]
	v_mfma_scale_f32_16x16x128_f8f6f4 v[44:47], v[16:23], v[226:233], v[44:47], v190, v191 op_sel_hi:[0,0,0]
	v_mfma_scale_f32_16x16x128_f8f6f4 v[36:39], v[24:31], v[226:233], v[36:39], v190, v191 op_sel_hi:[0,0,0]
	s_setprio 0
	s_setprio 1
	v_mfma_scale_f32_16x16x128_f8f6f4 v[88:91], v[0:7], v[202:209], v[88:91], v190, v191 op_sel_hi:[0,0,0]
	v_mfma_scale_f32_16x16x128_f8f6f4 v[80:83], v[8:15], v[202:209], v[80:83], v190, v191 op_sel_hi:[0,0,0]
	v_mfma_scale_f32_16x16x128_f8f6f4 v[72:75], v[0:7], v[210:217], v[72:75], v190, v191 op_sel_hi:[0,0,0]
	v_mfma_scale_f32_16x16x128_f8f6f4 v[64:67], v[8:15], v[210:217], v[64:67], v190, v191 op_sel_hi:[0,0,0]
	v_mfma_scale_f32_16x16x128_f8f6f4 v[56:59], v[0:7], v[218:225], v[56:59], v190, v191 op_sel_hi:[0,0,0]
	v_mfma_scale_f32_16x16x128_f8f6f4 v[48:51], v[8:15], v[218:225], v[48:51], v190, v191 op_sel_hi:[0,0,0]
	v_mfma_scale_f32_16x16x128_f8f6f4 v[40:43], v[0:7], v[226:233], v[40:43], v190, v191 op_sel_hi:[0,0,0]
	v_mfma_scale_f32_16x16x128_f8f6f4 v[32:35], v[8:15], v[226:233], v[32:35], v190, v191 op_sel_hi:[0,0,0]
	s_add_i32 s60, s60, 2
	s_add_u32 s30, s30, 0x100
	s_addc_u32 s31, s31, 0
	s_cmp_gt_u32 s60, 5
	s_setprio 0
	s_barrier
	s_cbranch_scc1 .LBB0_1109

.LBB0_1181:
	ds_read_b128 v[16:19], v193
	ds_read_b128 v[20:23], v193 offset:1024
	ds_read_b128 v[24:27], v193 offset:2048
	ds_read_b128 v[28:31], v193 offset:3072
	ds_read_b128 v[0:3], v194
	ds_read_b128 v[4:7], v194 offset:1024
	ds_read_b128 v[8:11], v194 offset:2048
	ds_read_b128 v[12:15], v194 offset:3072
	s_add_u32 s0, s28, 0x100
	s_addc_u32 s1, s29, 0
	s_cmp_eq_u32 s62, 18
	s_cselect_b32 s35, s25, s1
	s_cselect_b32 s34, s24, s0
	s_cselect_b32 s31, s27, s61
	s_cselect_b32 s30, s26, s60
	s_mov_b32 m0, s50
	v_lshl_add_u64 v[222:223], s[28:29], 0, v[176:177]
	ds_read_b128 v[178:181], v195
	ds_read_b128 v[182:185], v195 offset:1024
	ds_read_b128 v[198:201], v195 offset:2048
	ds_read_b128 v[202:205], v195 offset:3072
	ds_read_b128 v[206:209], v195 offset:4096
	ds_read_b128 v[210:213], v195 offset:5120
	ds_read_b128 v[214:217], v195 offset:6144
	ds_read_b128 v[218:221], v195 offset:7168
	global_load_lds_dwordx4 v[222:223], off
	v_lshl_add_u64 v[222:223], s[28:29], 0, v[174:175]
	s_mov_b32 m0, s51
	s_nop 0
	global_load_lds_dwordx4 v[222:223], off
	s_waitcnt vmcnt(8)
	s_waitcnt lgkmcnt(0)
	s_barrier
	s_setprio 1
	s_waitcnt lgkmcnt(0)
	v_mfma_scale_f32_16x16x128_f8f6f4 v[156:159], v[16:23], v[178:185], v[156:159], v188, v189 op_sel_hi:[0,0,0]
	v_mfma_scale_f32_16x16x128_f8f6f4 v[152:155], v[24:31], v[178:185], v[152:155], v188, v189 op_sel_hi:[0,0,0]
	v_mfma_scale_f32_16x16x128_f8f6f4 v[140:143], v[16:23], v[198:205], v[140:143], v188, v189 op_sel_hi:[0,0,0]
	v_mfma_scale_f32_16x16x128_f8f6f4 v[136:139], v[24:31], v[198:205], v[136:139], v188, v189 op_sel_hi:[0,0,0]
	v_mfma_scale_f32_16x16x128_f8f6f4 v[124:127], v[16:23], v[206:213], v[124:127], v188, v189 op_sel_hi:[0,0,0]
	v_mfma_scale_f32_16x16x128_f8f6f4 v[120:123], v[24:31], v[206:213], v[120:123], v188, v189 op_sel_hi:[0,0,0]
	v_mfma_scale_f32_16x16x128_f8f6f4 v[108:111], v[16:23], v[214:221], v[108:111], v188, v189 op_sel_hi:[0,0,0]
	v_mfma_scale_f32_16x16x128_f8f6f4 v[104:107], v[24:31], v[214:221], v[104:107], v188, v189 op_sel_hi:[0,0,0]
	s_setprio 0
	s_setprio 1
	v_mfma_scale_f32_16x16x128_f8f6f4 v[148:151], v[0:7], v[178:185], v[148:151], v188, v189 op_sel_hi:[0,0,0]
	v_mfma_scale_f32_16x16x128_f8f6f4 v[144:147], v[8:15], v[178:185], v[144:147], v188, v189 op_sel_hi:[0,0,0]
	v_mfma_scale_f32_16x16x128_f8f6f4 v[132:135], v[0:7], v[198:205], v[132:135], v188, v189 op_sel_hi:[0,0,0]
	v_mfma_scale_f32_16x16x128_f8f6f4 v[128:131], v[8:15], v[198:205], v[128:131], v188, v189 op_sel_hi:[0,0,0]
	v_mfma_scale_f32_16x16x128_f8f6f4 v[116:119], v[0:7], v[206:213], v[116:119], v188, v189 op_sel_hi:[0,0,0]
	v_mfma_scale_f32_16x16x128_f8f6f4 v[112:115], v[8:15], v[206:213], v[112:115], v188, v189 op_sel_hi:[0,0,0]
	v_mfma_scale_f32_16x16x128_f8f6f4 v[100:103], v[0:7], v[214:221], v[100:103], v188, v189 op_sel_hi:[0,0,0]
	v_mfma_scale_f32_16x16x128_f8f6f4 v[96:99], v[8:15], v[214:221], v[96:99], v188, v189 op_sel_hi:[0,0,0]
	s_setprio 0
	s_barrier
	s_mov_b32 m0, s52
	v_lshl_add_u64 v[184:185], s[30:31], 0, v[170:171]
	s_add_u32 s28, s30, 0x58000
	ds_read_b128 v[198:201], v195 offset:16384
	ds_read_b128 v[202:205], v195 offset:17408
	ds_read_b128 v[206:209], v195 offset:18432
	ds_read_b128 v[210:213], v195 offset:19456
	ds_read_b128 v[214:217], v195 offset:20480
	ds_read_b128 v[218:221], v195 offset:21504
	ds_read_b128 v[222:225], v195 offset:22528
	ds_read_b128 v[226:229], v195 offset:23552
	global_load_lds_dwordx4 v[184:185], off
	v_lshl_add_u64 v[182:183], s[30:31], 0, v[168:169]
	s_mov_b32 m0, s53
	s_addc_u32 s29, s31, 0
	global_load_lds_dwordx4 v[182:183], off
	v_lshl_add_u64 v[178:179], s[28:29], 0, v[170:171]
	s_mov_b32 m0, s54
	v_lshl_add_u64 v[180:181], s[34:35], 0, v[160:161]
	global_load_lds_dwordx4 v[178:179], off
	v_lshl_add_u64 v[178:179], s[28:29], 0, v[168:169]
	s_mov_b32 m0, s55
	s_nop 0
	global_load_lds_dwordx4 v[178:179], off
	v_lshl_add_u64 v[178:179], s[34:35], 0, v[164:165]
	s_mov_b32 m0, s39
	s_nop 0
	global_load_lds_dwordx4 v[178:179], off
	s_mov_b32 m0, s40
	s_nop 0
	global_load_lds_dwordx4 v[180:181], off
	s_waitcnt vmcnt(8)
	s_waitcnt lgkmcnt(0)
	s_barrier
	s_setprio 1
	s_waitcnt lgkmcnt(0)
	v_mfma_scale_f32_16x16x128_f8f6f4 v[92:95], v[16:23], v[198:205], v[92:95], v188, v189 op_sel_hi:[0,0,0]
	v_mfma_scale_f32_16x16x128_f8f6f4 v[88:91], v[24:31], v[198:205], v[88:91], v188, v189 op_sel_hi:[0,0,0]
	v_mfma_scale_f32_16x16x128_f8f6f4 v[76:79], v[16:23], v[206:213], v[76:79], v188, v189 op_sel_hi:[0,0,0]
	v_mfma_scale_f32_16x16x128_f8f6f4 v[72:75], v[24:31], v[206:213], v[72:75], v188, v189 op_sel_hi:[0,0,0]
	v_mfma_scale_f32_16x16x128_f8f6f4 v[60:63], v[16:23], v[214:221], v[60:63], v188, v189 op_sel_hi:[0,0,0]
	v_mfma_scale_f32_16x16x128_f8f6f4 v[56:59], v[24:31], v[214:221], v[56:59], v188, v189 op_sel_hi:[0,0,0]
	v_mfma_scale_f32_16x16x128_f8f6f4 v[44:47], v[16:23], v[222:229], v[44:47], v188, v189 op_sel_hi:[0,0,0]
	v_mfma_scale_f32_16x16x128_f8f6f4 v[40:43], v[24:31], v[222:229], v[40:43], v188, v189 op_sel_hi:[0,0,0]
	s_setprio 0
	s_setprio 1
	v_mfma_scale_f32_16x16x128_f8f6f4 v[84:87], v[0:7], v[198:205], v[84:87], v188, v189 op_sel_hi:[0,0,0]
	v_mfma_scale_f32_16x16x128_f8f6f4 v[80:83], v[8:15], v[198:205], v[80:83], v188, v189 op_sel_hi:[0,0,0]
	v_mfma_scale_f32_16x16x128_f8f6f4 v[68:71], v[0:7], v[206:213], v[68:71], v188, v189 op_sel_hi:[0,0,0]
	v_mfma_scale_f32_16x16x128_f8f6f4 v[64:67], v[8:15], v[206:213], v[64:67], v188, v189 op_sel_hi:[0,0,0]
	v_mfma_scale_f32_16x16x128_f8f6f4 v[52:55], v[0:7], v[214:221], v[52:55], v188, v189 op_sel_hi:[0,0,0]
	v_mfma_scale_f32_16x16x128_f8f6f4 v[48:51], v[8:15], v[214:221], v[48:51], v188, v189 op_sel_hi:[0,0,0]
	v_mfma_scale_f32_16x16x128_f8f6f4 v[36:39], v[0:7], v[222:229], v[36:39], v188, v189 op_sel_hi:[0,0,0]
	v_mfma_scale_f32_16x16x128_f8f6f4 v[32:35], v[8:15], v[222:229], v[32:35], v188, v189 op_sel_hi:[0,0,0]
	s_setprio 0
	s_barrier
	s_add_i32 s63, 0, 0x1c000
	v_add_u32_e32 v28, s63, v191
	ds_read_b128 v[0:3], v196
	ds_read_b128 v[4:7], v196 offset:1024
	ds_read_b128 v[8:11], v196 offset:2048
	ds_read_b128 v[12:15], v196 offset:3072
	ds_read_b128 v[16:19], v28
	ds_read_b128 v[20:23], v28 offset:1024
	ds_read_b128 v[24:27], v28 offset:2048
	ds_read_b128 v[28:31], v28 offset:3072
	s_mov_b32 m0, s41
	v_lshl_add_u64 v[230:231], s[34:35], 0, v[166:167]
	ds_read_b128 v[198:201], v195 offset:32768
	ds_read_b128 v[202:205], v195 offset:33792
	ds_read_b128 v[206:209], v195 offset:34816
	ds_read_b128 v[210:213], v195 offset:35840
	ds_read_b128 v[214:217], v195 offset:36864
	ds_read_b128 v[218:221], v195 offset:37888
	ds_read_b128 v[222:225], v195 offset:38912
	ds_read_b128 v[226:229], v195 offset:39936
	global_load_lds_dwordx4 v[230:231], off
	v_lshl_add_u64 v[230:231], s[34:35], 0, v[162:163]
	s_mov_b32 m0, s42
	s_nop 0
	global_load_lds_dwordx4 v[230:231], off
	s_waitcnt vmcnt(8)
	s_waitcnt lgkmcnt(0)
	s_barrier
	s_setprio 1
	s_waitcnt lgkmcnt(0)
	v_mfma_scale_f32_16x16x128_f8f6f4 v[156:159], v[0:7], v[198:205], v[156:159], v188, v189 op_sel_hi:[0,0,0]
	v_mfma_scale_f32_16x16x128_f8f6f4 v[152:155], v[8:15], v[198:205], v[152:155], v188, v189 op_sel_hi:[0,0,0]
	v_mfma_scale_f32_16x16x128_f8f6f4 v[140:143], v[0:7], v[206:213], v[140:143], v188, v189 op_sel_hi:[0,0,0]
	v_mfma_scale_f32_16x16x128_f8f6f4 v[136:139], v[8:15], v[206:213], v[136:139], v188, v189 op_sel_hi:[0,0,0]
	v_mfma_scale_f32_16x16x128_f8f6f4 v[124:127], v[0:7], v[214:221], v[124:127], v188, v189 op_sel_hi:[0,0,0]
	v_mfma_scale_f32_16x16x128_f8f6f4 v[120:123], v[8:15], v[214:221], v[120:123], v188, v189 op_sel_hi:[0,0,0]
	v_mfma_scale_f32_16x16x128_f8f6f4 v[108:111], v[0:7], v[222:229], v[108:111], v188, v189 op_sel_hi:[0,0,0]
	v_mfma_scale_f32_16x16x128_f8f6f4 v[104:107], v[8:15], v[222:229], v[104:107], v188, v189 op_sel_hi:[0,0,0]
	s_setprio 0
	s_setprio 1
	v_mfma_scale_f32_16x16x128_f8f6f4 v[148:151], v[16:23], v[198:205], v[148:151], v188, v189 op_sel_hi:[0,0,0]
	v_mfma_scale_f32_16x16x128_f8f6f4 v[144:147], v[24:31], v[198:205], v[144:147], v188, v189 op_sel_hi:[0,0,0]
	v_mfma_scale_f32_16x16x128_f8f6f4 v[132:135], v[16:23], v[206:213], v[132:135], v188, v189 op_sel_hi:[0,0,0]
	v_mfma_scale_f32_16x16x128_f8f6f4 v[128:131], v[24:31], v[206:213], v[128:131], v188, v189 op_sel_hi:[0,0,0]
	v_mfma_scale_f32_16x16x128_f8f6f4 v[116:119], v[16:23], v[214:221], v[116:119], v188, v189 op_sel_hi:[0,0,0]
	v_mfma_scale_f32_16x16x128_f8f6f4 v[112:115], v[24:31], v[214:221], v[112:115], v188, v189 op_sel_hi:[0,0,0]
	v_mfma_scale_f32_16x16x128_f8f6f4 v[100:103], v[16:23], v[222:229], v[100:103], v188, v189 op_sel_hi:[0,0,0]
	v_mfma_scale_f32_16x16x128_f8f6f4 v[96:99], v[24:31], v[222:229], v[96:99], v188, v189 op_sel_hi:[0,0,0]
	s_setprio 0
	s_barrier
	s_add_i32 s28, s56, s38
	v_lshl_add_u64 v[184:185], v[184:185], 0, s[12:13]
	s_mov_b32 m0, s28
	ds_read_b128 v[198:201], v195 offset:49152
	ds_read_b128 v[202:205], v195 offset:50176
	ds_read_b128 v[206:209], v195 offset:51200
	ds_read_b128 v[210:213], v195 offset:52224
	ds_read_b128 v[214:217], v195 offset:53248
	ds_read_b128 v[218:221], v195 offset:54272
	ds_read_b128 v[222:225], v195 offset:55296
	ds_read_b128 v[226:229], v195 offset:56320
	global_load_lds_dwordx4 v[184:185], off
	s_add_i32 m0, s28, 0x2000
	s_add_u32 s28, s30, 0x58080
	v_lshl_add_u64 v[182:183], v[182:183], 0, s[12:13]
	s_addc_u32 s29, s31, 0
	s_add_i32 s30, s63, s38
	global_load_lds_dwordx4 v[182:183], off
	v_lshl_add_u64 v[182:183], s[28:29], 0, v[170:171]
	s_mov_b32 m0, s30
	v_lshl_add_u64 v[178:179], v[178:179], 0, s[12:13]
	global_load_lds_dwordx4 v[182:183], off
	v_lshl_add_u64 v[182:183], s[28:29], 0, v[168:169]
	s_add_i32 m0, s30, 0x2000
	s_nop 0
	global_load_lds_dwordx4 v[182:183], off
	s_mov_b32 m0, s45
	s_nop 0
	global_load_lds_dwordx4 v[178:179], off
	v_lshl_add_u64 v[178:179], v[180:181], 0, s[12:13]
	s_mov_b32 m0, s46
	s_nop 0
	global_load_lds_dwordx4 v[178:179], off
	s_waitcnt vmcnt(8)
	s_waitcnt lgkmcnt(0)
	s_barrier
	s_setprio 1
	s_waitcnt lgkmcnt(0)
	v_mfma_scale_f32_16x16x128_f8f6f4 v[92:95], v[0:7], v[198:205], v[92:95], v188, v189 op_sel_hi:[0,0,0]
	v_mfma_scale_f32_16x16x128_f8f6f4 v[88:91], v[8:15], v[198:205], v[88:91], v188, v189 op_sel_hi:[0,0,0]
	v_mfma_scale_f32_16x16x128_f8f6f4 v[76:79], v[0:7], v[206:213], v[76:79], v188, v189 op_sel_hi:[0,0,0]
	v_mfma_scale_f32_16x16x128_f8f6f4 v[72:75], v[8:15], v[206:213], v[72:75], v188, v189 op_sel_hi:[0,0,0]
	v_mfma_scale_f32_16x16x128_f8f6f4 v[60:63], v[0:7], v[214:221], v[60:63], v188, v189 op_sel_hi:[0,0,0]
	v_mfma_scale_f32_16x16x128_f8f6f4 v[56:59], v[8:15], v[214:221], v[56:59], v188, v189 op_sel_hi:[0,0,0]
	v_mfma_scale_f32_16x16x128_f8f6f4 v[44:47], v[0:7], v[222:229], v[44:47], v188, v189 op_sel_hi:[0,0,0]
	v_mfma_scale_f32_16x16x128_f8f6f4 v[40:43], v[8:15], v[222:229], v[40:43], v188, v189 op_sel_hi:[0,0,0]
	s_setprio 0
	s_setprio 1
	v_mfma_scale_f32_16x16x128_f8f6f4 v[84:87], v[16:23], v[198:205], v[84:87], v188, v189 op_sel_hi:[0,0,0]
	v_mfma_scale_f32_16x16x128_f8f6f4 v[80:83], v[24:31], v[198:205], v[80:83], v188, v189 op_sel_hi:[0,0,0]
	v_mfma_scale_f32_16x16x128_f8f6f4 v[68:71], v[16:23], v[206:213], v[68:71], v188, v189 op_sel_hi:[0,0,0]
	v_mfma_scale_f32_16x16x128_f8f6f4 v[64:67], v[24:31], v[206:213], v[64:67], v188, v189 op_sel_hi:[0,0,0]
	v_mfma_scale_f32_16x16x128_f8f6f4 v[52:55], v[16:23], v[214:221], v[52:55], v188, v189 op_sel_hi:[0,0,0]
	v_mfma_scale_f32_16x16x128_f8f6f4 v[48:51], v[24:31], v[214:221], v[48:51], v188, v189 op_sel_hi:[0,0,0]
	v_mfma_scale_f32_16x16x128_f8f6f4 v[36:39], v[16:23], v[222:229], v[36:39], v188, v189 op_sel_hi:[0,0,0]
	v_mfma_scale_f32_16x16x128_f8f6f4 v[32:35], v[24:31], v[222:229], v[32:35], v188, v189 op_sel_hi:[0,0,0]
	s_add_i32 s62, s62, 2
	s_add_u32 s60, s60, 0x100
	s_addc_u32 s61, s61, 0
	s_cmp_gt_u32 s62, 19
	s_mov_b64 s[28:29], s[0:1]
	s_setprio 0
	s_barrier
	s_cbranch_scc0 .LBB0_1181
	s_and_b64 vcc, exec, s[14:15]
	s_cbranch_vccz .LBB0_1184
	s_barrier
